# P5: attention workgroups raise the converters' stop flag two key tiles before the end of their last block (plus the P1 early flag)
# speedup vs baseline: 1.0032x; 1.0010x over previous
; #define LAS __attribute__((address_space(3)))
; __device__ __forceinline__ void attn_unit(LAS unsigned char* lds, int b, int h, int qb, int ta, int tb, const bf16* __restrict__ Q, const bf16* __restrict__ Kn, const bf16* __restrict__ Kpe, ...
;     const int tid = threadIdx.x, lane = tid & 63, r32 = lane & 31, hi = lane >> 5, wid = __builtin_amdgcn_readfirstlane(tid >> 6);
;     const int t0 = qb * 256 + wid * 32;
;     const int m0 = b * S + t0;
;     const int wave_max_pos = t0 + 31 + NMETA, wave_min_pos = t0 + NMETA;
;     LAS float* wsf = (LAS float*)(lds + WSF_OFF) + wid * 64;
;     unsigned koff[3], kdst[3], kstr[3];
; #pragma unroll
;     for (int i = 0; i < 3; ++i) { const int id = tid + 512 * i, key = id / 24, c = id % 24;
;         koff[i] = c < 16 ? (unsigned)((((b * LP + key) * NH + h) * 128 + c * 8) * 2) : (unsigned)(WS_KPE - WS_KN) + (unsigned)(((b * LP + key) * ROPE + (c - 16) * 8) * 2);
;         kstr[i] = c < 16 ? 64u * NH * 128 * 2 : 64u * ROPE * 2;
;         const int row = (key & ~12) | ((key & 4) << 1) | ((key & 8) >> 1);
;         kdst[i] = (unsigned)(row * KPITCH + c * 16); }
;     unsigned voff[2], vdst[2];
; #pragma unroll
;     for (int i = 0; i < 2; ++i) { const int id = tid + 512 * i, d = id >> 3, kc = id & 7;
;         voff[i] = (unsigned)((((b * NH + h) * 128 + d) * LP + kc * 8) * 2); vdst[i] = (unsigned)(KBYTES + d * VPITCH + kc * 16); }
; __device__ __forceinline__ void phase5() { const Ctx c = make_ctx(); PHASE_PTRS;
;     ...
;             for (int u = c.wg; u < NB * NH * 16; u += c.G) { const int bh = u >> 4, qb = u & 15; att::attn_unit(c.lds, bh >> 3, bh & 7, qb, 0, 4 * qb + 5, Q, Kn, Kpe, V, INP(10), mixed); }
;         } else if ((c.wg >> 3) < 16) {
;             const int x = c.wg & 7, i = c.wg >> 3;
; #pragma unroll 1
;             for (int k = 0; k < 2; ++k) { const int bh = 2 * x + k, qb = k == 0 ? i : 15 - i;
;                 att::attn_unit(c.lds, bh >> 3, bh & 7, qb, 0, 4 * qb + 5, Q, Kn, Kpe, V, INP(10), mixed); }
.LBB0_960:
	v_readlane_b32 s0, v252, 0
	v_readlane_b32 s1, v252, 1
	s_cmp_lt_i32 s0, 6
	s_cselect_b64 s[4:5], -1, 0
	s_cmp_gt_i32 s1, 5
	s_cselect_b64 s[6:7], -1, 0
	s_and_b64 s[4:5], s[4:5], s[6:7]
	s_andn2_b64 vcc, exec, s[4:5]
	s_cbranch_vccnz .LBB0_1024
	s_mov_b32 s97, 0
	v_mov_b32_e32 v1, v0
	s_mov_b64 s[38:39], s[94:95]
	s_load_dwordx2 s[16:17], s[38:39], 0xa8
	v_readlane_b32 s0, v252, 6
	v_readlane_b32 s1, v252, 7
	s_mov_b64 s[4:5], -1
	s_waitcnt lgkmcnt(0)
	s_add_u32 s28, s16, 0x38200000
	s_addc_u32 s29, s17, 0
	s_add_u32 s36, s16, 0x3e000000
	s_addc_u32 s37, s17, 0
	s_add_u32 s30, s16, 1.0
	s_addc_u32 s31, s17, 0
	s_add_u32 s34, s16, 0x40a00000
	s_addc_u32 s35, s17, 0
	s_andn2_b64 vcc, exec, s[0:1]
	s_cbranch_vccnz .LBB0_996
	s_cmpk_gt_i32 s2, 0xff
	s_cbranch_scc1 .LBB0_995
	v_mul_u32_u24_e32 v1, 0xaab, v0
	s_waitcnt vmcnt(0)
	v_mov_b32_e32 v2, 24
	v_mul_lo_u16_sdwa v3, v1, v2 dst_sel:DWORD dst_unused:UNUSED_PAD src0_sel:WORD_1 src1_sel:DWORD
	v_sub_u16_e32 v3, v0, v3
	v_cmp_lt_u16_e64 s[4:5], 15, v3
	v_lshlrev_b16_e32 v183, 4, v3
	v_mov_b32_e32 v3, 19
	v_lshrrev_b32_e32 v4, 15, v1
	v_lshrrev_b32_e32 v5, 17, v1
	v_and_b32_sdwa v3, v1, v3 dst_sel:DWORD dst_unused:UNUSED_PAD src0_sel:WORD_1 src1_sel:DWORD
	v_and_b32_e32 v4, 8, v4
	v_and_b32_e32 v5, 4, v5
	v_or3_b32 v4, v3, v4, v5
	v_or_b32_e32 v3, 0x200, v0
	v_mul_u32_u24_e32 v189, 0xaab, v3
	v_mul_lo_u16_sdwa v5, v189, v2 dst_sel:DWORD dst_unused:UNUSED_PAD src0_sel:WORD_1 src1_sel:DWORD
	v_sub_u16_e32 v5, v3, v5
	v_cmp_lt_u16_e64 s[6:7], 15, v5
	v_lshlrev_b16_e32 v190, 4, v5
	v_mov_b32_e32 v5, 51
	v_lshrrev_b32_e32 v7, 15, v189
	v_lshrrev_b32_e32 v8, 17, v189
	v_and_b32_sdwa v6, v189, v5 dst_sel:DWORD dst_unused:UNUSED_PAD src0_sel:WORD_1 src1_sel:DWORD
	v_and_b32_e32 v7, 8, v7
	v_and_b32_e32 v8, 4, v8
	s_movk_i32 s8, 0xaab
	v_or3_b32 v6, v6, v7, v8
	v_or_b32_e32 v7, 0x400, v0
	v_mul_u32_u24_sdwa v192, v7, s8 dst_sel:DWORD dst_unused:UNUSED_PAD src0_sel:WORD_0 src1_sel:DWORD
	v_mul_lo_u16_sdwa v2, v192, v2 dst_sel:DWORD dst_unused:UNUSED_PAD src0_sel:WORD_1 src1_sel:DWORD
	v_sub_u16_e32 v2, v7, v2
	v_cmp_lt_u16_e64 s[8:9], 15, v2
	v_lshlrev_b16_e32 v193, 4, v2
	v_and_b32_sdwa v2, v192, v5 dst_sel:DWORD dst_unused:UNUSED_PAD src0_sel:WORD_1 src1_sel:DWORD
	v_lshrrev_b32_e32 v5, 15, v192
	v_lshrrev_b32_e32 v7, 17, v192
	s_load_dwordx2 s[40:41], s[38:39], 0x50
	v_and_b32_e32 v5, 8, v5
	v_and_b32_e32 v7, 4, v7
	v_or3_b32 v2, v2, v5, v7
	v_lshlrev_b32_e32 v5, 4, v0
	v_and_b32_e32 v195, 0x70, v5
	v_lshrrev_b32_e32 v197, 3, v3
	v_bfe_u32 v5, v0, 5, 1
	v_mov_b32_e32 v3, 0
	s_movk_i32 s12, 0x190
	v_and_b32_e32 v182, 31, v0
	v_lshrrev_b32_e32 v196, 3, v0
	v_lshlrev_b32_e32 v184, 4, v5
	v_mov_b32_e32 v185, v3
	s_movk_i32 s10, 0x90
	v_mad_u32_u24 v203, v4, s12, v183
	v_mad_u32_u24 v204, v6, s12, v190
	v_mad_u32_u24 v205, v2, s12, v193
	v_mbcnt_lo_u32_b32 v2, -1, 0
	v_add_u32_e32 v188, 0x23fff00, v183
	v_add_u32_e32 v191, 0x23fff00, v190
	v_add_u32_e32 v194, 0x23fff00, v193
	v_lshlrev_b32_e32 v198, 3, v5
	v_lshl_add_u64 v[186:187], s[36:37], 0, v[184:185]
	v_mad_u32_u24 v185, v196, s10, v195
	v_mad_u32_u24 v199, v197, s10, v195
	v_mul_u32_u24_e32 v200, 0x190, v182
	s_mov_b32 s43, 0
	v_cmp_eq_u32_e64 s[10:11], 0, v5
	v_mul_u32_u24_e32 v201, 0x90, v182
	v_lshlrev_b32_e32 v202, 2, v5
	v_or_b32_e32 v206, 0x80, v195
	s_movk_i32 s24, 0x2100
	s_movk_i32 s25, 0x180
	v_add_u32_e32 v207, 0, v203
	v_add_u32_e32 v208, 0, v204
	s_mov_b32 s26, 0x41000000
	v_mbcnt_hi_u32_b32 v209, -1, v2
	s_brev_b32 s44, 60
	s_mov_b32 s46, 0x358637bd
	s_mov_b32 s27, 0x800000
	s_movk_i32 s45, 0x7fff
	v_add_u32_e32 v210, 0, v205
	v_mov_b32_e32 v211, 0xff800000
	s_mov_b32 s47, s2
	s_mov_b32 s48, s2
	s_branch .LBB0_965

; __device__ __forceinline__ void attn_unit(LAS unsigned char* lds, int b, int h, int qb, int ta, int tb, const bf16* __restrict__ Q, const bf16* __restrict__ Kn, const bf16* __restrict__ Kpe, ...
;     ...
;     for (int t = ta; t < tb; ++t) {
;         const bool more = t + 1 < tb; const int st = (t - ta) & 1;
;         if (more) {
; #pragma unroll
;             for (int i = 0; i < 3; ++i) kreg[i] = *(const u32x4*)(Knb + (koff[i] + (unsigned)(t + 1) * kstr[i]));
; #pragma unroll
;             for (int i = 0; i < 2; ++i) vreg[i] = *(const u32x4*)(Vtb + (voff[i] + (unsigned)(t + 1) * 128u));
;         }
;         const int kb = t * 64;
;         if (kb <= wave_max_pos) {
; __device__ __forceinline__ void phase5() { const Ctx c = make_ctx(); PHASE_PTRS;
;     ...
;             for (int k = 0; k < 2; ++k) { const int bh = 2 * x + k, qb = k == 0 ? i : 15 - i;
;                 att::attn_unit(c.lds, bh >> 3, bh & 7, qb, 0, 4 * qb + 5, Q, Kn, Kpe, V, INP(10), mixed); }
;             const Ctx c3 = make_ctx(); if (c3.tid == 0) __hip_atomic_fetch_add(ctl + CW_ADONE, 1u, __ATOMIC_RELAXED, __HIP_MEMORY_SCOPE_AGENT);
.LBB0_1015:
	s_sub_i32 s98, s50, s53
	s_cmp_eq_u32 s98, 2
	s_cbranch_scc0 .Lp5sig_skip
	s_and_b64 s[98:99], s[12:13], exec
	s_cbranch_scc1 .Lp5sig_skip
	v_readfirstlane_b32 s98, v0
	s_cmp_lg_u32 s98, 0
	s_cbranch_scc1 .Lp5sig_skip
	s_mov_b64 s[98:99], exec
	s_mov_b64 exec, 1
	v_mov_b32_e32 v253, 0x1000
	v_mov_b32_e32 v254, 1
	global_atomic_add v253, v254, s[16:17] offset:1024
	s_mov_b64 exec, s[98:99]
	s_mov_b32 s97, 1

; __device__ __forceinline__ void phase5() { const Ctx c = make_ctx(); PHASE_PTRS;
;     ...
;             const Ctx c3 = make_ctx(); if (c3.tid == 0) __hip_atomic_fetch_add(ctl + CW_ADONE, 1u, __ATOMIC_RELAXED, __HIP_MEMORY_SCOPE_AGENT);
.LBB0_1020:
	v_mov_b32_e32 v1, v0
	s_nop 0
	v_cmp_eq_u32_e32 vcc, 0, v1
	s_and_saveexec_b64 s[4:5], vcc
	s_cbranch_execz .LBB0_1023
	s_mov_b64 s[6:7], exec
	v_mbcnt_lo_u32_b32 v1, s6, 0
	v_mbcnt_hi_u32_b32 v1, s7, v1
	v_cmp_eq_u32_e32 vcc, 0, v1
	s_and_b64 s[8:9], exec, vcc
	s_mov_b64 exec, s[8:9]
	s_cbranch_execz .LBB0_1023
	s_bcnt1_i32_b64 s6, s[6:7]
	v_mov_b32_e32 v1, 0x1000
	v_mov_b32_e32 v2, s6
	s_cmp_lg_u32 s97, 0
	s_cbranch_scc1 .Lp5sig_fin
	global_atomic_add v1, v2, s[16:17] offset:1024
.Lp5sig_fin:
.LBB0_1023:
	s_or_b64 exec, exec, s[4:5]
